# sc1 write-through also on level-0 outputs and weight-transpose dwordx4 stores
# baseline (speedup 1.0000x reference)
_Z12front_kernelPKiS0_S0_PKfS2_S2_S2_S2_Pc:
	s_load_dwordx2 s[28:29], s[0:1], 0x40
	s_load_dwordx2 s[18:19], s[0:1], 0x8
	s_cmp_gt_i32 s2, 31
	s_mov_b64 s[4:5], -1
	s_cbranch_scc0 .LBB0_30
	s_load_dwordx2 s[20:21], s[0:1], 0x20
	s_load_dwordx2 s[22:23], s[0:1], 0x30
	s_cmp_lg_u32 s2, 32
	s_cbranch_scc0 .LBB0_17
	s_cmp_lt_u32 s2, 40
	s_cbranch_scc1 .LBB0_16
	s_load_dwordx2 s[24:25], s[0:1], 0x18
	s_load_dwordx2 s[26:27], s[0:1], 0x28
	s_cmpk_gt_u32 s2, 0x427
	s_cbranch_scc0 .LBB0_9
	s_load_dwordx2 s[4:5], s[0:1], 0x0
	s_lshl_b32 s3, s2, 1
	s_add_i32 s3, s3, 0x7ffff7b0
	s_and_b32 s3, s3, 0x7ffffff0
	v_lshrrev_b32_e32 v1, 4, v0
	v_or_b32_e32 v8, s3, v1
	v_lshlrev_b32_e32 v6, 2, v8
	v_mov_b32_e32 v7, 0
	s_waitcnt lgkmcnt(0)
	v_lshl_add_u64 v[2:3], v[6:7], 2, s[4:5]
	v_lshlrev_b32_e32 v6, 1, v8
	v_lshl_add_u64 v[10:11], v[6:7], 2, s[18:19]
	global_load_dwordx4 v[2:5], v[2:3], off
	v_mov_b32_e32 v9, v7
	global_load_dwordx2 v[10:11], v[10:11], off
	s_lshl_b32 s4, s2, 7
	v_lshlrev_b32_e32 v1, 3, v0
	s_mov_b32 s5, 0x20000
	v_lshl_add_u64 v[16:17], v[8:9], 2, s[18:19]
	v_and_b32_e32 v1, 0x78, v1
	s_and_b32 s4, s4, 0x380
	v_add_co_u32_e32 v16, vcc, s5, v16
	s_movk_i32 s8, 0x3e9
	v_or_b32_e32 v64, s4, v1
	s_add_u32 s4, s26, 0x3d2844
	v_addc_co_u32_e32 v17, vcc, 0, v17, vcc
	s_addc_u32 s6, s27, 0
	v_mov_b32_e32 v32, s4
	global_load_dword v65, v[16:17], off
	v_mov_b32_e32 v33, s6
	v_mov_b32_e32 v18, s27
	v_mov_b32_e32 v19, s26
	v_mov_b32_e32 v13, v7
	v_mov_b32_e32 v30, s23
	v_mov_b32_e32 v31, s22
	s_movk_i32 s3, 0xfa4
	v_min_u32_e32 v1, 0x3e1, v64
	v_mov_b32_e32 v15, v7
	s_movk_i32 s16, 0x3e8
	v_cmp_eq_u32_e64 s[16:17], s16, v64
	v_lshlrev_b64 v[8:9], 12, v[8:9]
	v_lshl_add_u64 v[8:9], s[28:29], 0, v[8:9]
	s_waitcnt vmcnt(2)
	v_cmp_gt_u32_e64 s[4:5], s8, v2
	s_nop 1
	v_cndmask_b32_e64 v16, 0, v2, s[4:5]
	s_waitcnt vmcnt(1)
	v_cmp_eq_u32_e64 s[10:11], 1, v10
	v_cmp_gt_u32_e64 s[6:7], s8, v3
	v_cmp_gt_u32_e32 vcc, s8, v4
	v_cndmask_b32_e64 v2, 2, 1, s[10:11]
	v_cmp_eq_u32_e64 s[10:11], 1, v11
	v_cndmask_b32_e64 v17, 0, v3, s[6:7]
	v_cndmask_b32_e32 v34, 0, v4, vcc
	v_cndmask_b32_e64 v3, 2, 1, s[10:11]
	v_cmp_ne_u32_e64 s[10:11], 0, v11
	v_cmp_gt_u32_e64 s[8:9], s8, v5
	s_nop 0
	v_cndmask_b32_e64 v20, 0, v3, s[10:11]
	v_cmp_ne_u32_e64 s[10:11], 0, v10
	v_mul_u32_u24_e32 v12, 0xf4a11, v20
	v_cndmask_b32_e64 v35, 0, v5, s[8:9]
	v_cndmask_b32_e64 v4, 0, v2, s[10:11]
	v_mul_u32_u24_e32 v6, 0xf4a11, v4
	v_lshl_add_u64 v[2:3], v[6:7], 2, s[24:25]
	v_mul_u32_u24_e32 v6, 0x3e9, v4
	v_cmp_eq_u32_e64 s[10:11], 2, v4
	v_lshl_add_u64 v[22:23], v[12:13], 2, s[24:25]
	v_lshl_add_u64 v[10:11], v[6:7], 2, s[20:21]
	v_cndmask_b32_e64 v5, v3, v18, s[10:11]
	v_cndmask_b32_e64 v4, v2, v19, s[10:11]
	v_cmp_eq_u32_e64 s[12:13], 2, v20
	v_mul_u32_u24_e32 v14, 0x3e9, v20
	v_cndmask_b32_e64 v3, v3, v33, s[10:11]
	v_cndmask_b32_e64 v2, v2, v32, s[10:11]
	v_lshlrev_b32_e32 v6, 2, v1
	v_cndmask_b32_e64 v27, v23, v18, s[12:13]
	v_cndmask_b32_e64 v26, v22, v19, s[12:13]
	v_cndmask_b32_e64 v11, v11, v30, s[10:11]
	v_cndmask_b32_e64 v10, v10, v31, s[10:11]
	v_mad_i64_i32 v[4:5], s[10:11], v16, s3, v[4:5]
	v_lshl_add_u64 v[24:25], v[14:15], 2, s[20:21]
	v_mad_i64_i32 v[2:3], s[10:11], v17, s3, v[2:3]
	v_lshl_add_u64 v[54:55], v[4:5], 0, v[6:7]
	v_cndmask_b32_e64 v23, v23, v33, s[12:13]
	v_cndmask_b32_e64 v22, v22, v32, s[12:13]
	v_mad_i64_i32 v[26:27], s[10:11], v34, s3, v[26:27]
	v_lshl_add_u64 v[56:57], v[2:3], 0, v[6:7]
	v_lshl_add_u64 v[28:29], v[10:11], 0, v[6:7]
	global_load_dwordx4 v[2:5], v[54:55], off
	global_load_dwordx4 v[10:13], v[56:57], off
	global_load_dwordx4 v[14:17], v[28:29], off offset:16
	global_load_dwordx4 v[18:21], v[28:29], off
	v_cndmask_b32_e64 v25, v25, v30, s[12:13]
	v_cndmask_b32_e64 v24, v24, v31, s[12:13]
	v_mad_i64_i32 v[22:23], s[10:11], v35, s3, v[22:23]
	v_lshl_add_u64 v[60:61], v[26:27], 0, v[6:7]
	v_lshl_add_u64 v[58:59], v[24:25], 0, v[6:7]
	v_lshl_add_u64 v[62:63], v[22:23], 0, v[6:7]
	global_load_dwordx4 v[22:25], v[60:61], off
	global_load_dwordx4 v[26:29], v[62:63], off
	global_load_dwordx4 v[30:33], v[58:59], off
	global_load_dwordx4 v[34:37], v[58:59], off offset:16
	global_load_dwordx4 v[38:41], v[54:55], off offset:16
	global_load_dwordx4 v[42:45], v[56:57], off offset:16
	global_load_dwordx4 v[46:49], v[60:61], off offset:16
	global_load_dwordx4 v[50:53], v[62:63], off offset:16
	s_movk_i32 s3, 0x3e2
	v_cmp_gt_u32_e64 s[10:11], s3, v64
	s_and_b64 s[12:13], s[4:5], s[10:11]
	s_and_b64 s[14:15], s[6:7], s[10:11]
	s_waitcnt vmcnt(11)
	v_cndmask_b32_e64 v1, 0, v2, s[10:11]
	s_waitcnt vmcnt(10)
	v_cndmask_b32_e64 v2, 0, v10, s[10:11]
	v_cndmask_b32_e64 v3, 0, v3, s[12:13]
	s_waitcnt vmcnt(8)
	v_cndmask_b32_e64 v10, 0, v19, s[10:11]
	v_cndmask_b32_e64 v19, 0, v21, s[10:11]
	v_cndmask_b32_e64 v11, 0, v11, s[14:15]
	s_waitcnt vmcnt(7)
	v_cndmask_b32_e64 v21, 0, v22, s[10:11]
	s_waitcnt vmcnt(6)
	v_cndmask_b32_e64 v22, 0, v26, s[10:11]
	s_waitcnt vmcnt(3)
	v_cndmask_b32_e64 v1, v1, v41, s[16:17]
	s_waitcnt vmcnt(2)
	v_cndmask_b32_e64 v2, v2, v45, s[16:17]
	v_add_f32_e32 v3, v3, v11
	v_cndmask_b32_e64 v4, 0, v4, s[12:13]
	v_cndmask_b32_e64 v11, 0, v12, s[14:15]
	v_cndmask_b32_e64 v5, 0, v5, s[12:13]
	v_cndmask_b32_e64 v12, 0, v13, s[14:15]
	v_cndmask_b32_e64 v13, 0, v38, s[12:13]
	v_cndmask_b32_e64 v38, 0, v39, s[12:13]
	v_cndmask_b32_e64 v39, 0, v43, s[14:15]
	s_waitcnt vmcnt(1)
	v_cndmask_b32_e64 v21, v21, v49, s[16:17]
	s_waitcnt vmcnt(0)
	v_cndmask_b32_e64 v22, v22, v53, s[16:17]
	v_cndmask_b32_e64 v6, 0, v18, s[10:11]
	v_cndmask_b32_e64 v18, 0, v20, s[10:11]
	v_cndmask_b32_e64 v15, 0, v15, s[10:11]
	v_cndmask_b32_e64 v26, 0, v30, s[10:11]
	v_cndmask_b32_e64 v1, 0, v1, s[4:5]
	v_cndmask_b32_e64 v2, 0, v2, s[6:7]
	v_add_f32_e32 v3, v10, v3
	v_add_f32_e32 v10, v4, v11
	v_add_f32_e32 v5, v5, v12
	v_add_f32_e32 v12, v38, v39
	v_cndmask_b32_e32 v21, 0, v21, vcc
	v_cndmask_b32_e64 v22, 0, v22, s[8:9]
	v_cndmask_b32_e64 v6, v6, v17, s[16:17]
	v_cndmask_b32_e64 v26, v26, v37, s[16:17]
	v_add_f32_e32 v1, v1, v2
	v_add_f32_e32 v2, v18, v10
	v_add_f32_e32 v12, v15, v12
	v_add_f32_e32 v15, v21, v22
	v_max_f32_e32 v4, 0, v3
	v_add_f32_e32 v3, v19, v5
	v_add_f32_e32 v6, v6, v1
	v_max_f32_e32 v5, 0, v2
	v_max_f32_e32 v2, 0, v12
	v_add_f32_e32 v12, v26, v15
	s_and_b64 vcc, vcc, s[10:11]
	s_and_b64 s[4:5], s[8:9], s[10:11]
	v_cndmask_b32_e64 v20, 0, v17, s[10:11]
	v_cndmask_b32_e64 v17, 0, v42, s[14:15]
	v_cndmask_b32_e64 v40, 0, v40, s[12:13]
	v_cndmask_b32_e64 v42, 0, v44, s[14:15]
	v_max_f32_e32 v18, 0, v6
	v_max_f32_e32 v19, 0, v12
	v_cndmask_b32_e32 v6, 0, v23, vcc
	v_cndmask_b32_e64 v12, 0, v27, s[4:5]
	v_cndmask_b32_e64 v16, 0, v16, s[10:11]
	v_cndmask_b32_e64 v30, 0, v31, s[10:11]
	v_add_f32_e32 v11, v13, v17
	v_add_f32_e32 v13, v40, v42
	v_add_f32_e32 v6, v6, v12
	v_add_f32_e32 v13, v16, v13
	v_add_f32_e32 v6, v30, v6
	v_cndmask_b32_e64 v41, 0, v41, s[12:13]
	v_cndmask_b32_e64 v43, 0, v45, s[14:15]
	v_max_f32_e32 v10, 0, v3
	v_max_f32_e32 v3, 0, v13
	v_max_f32_e32 v12, 0, v6
	v_cndmask_b32_e32 v6, 0, v24, vcc
	v_cndmask_b32_e64 v13, 0, v28, s[4:5]
	v_cndmask_b32_e64 v14, 0, v14, s[10:11]
	v_cndmask_b32_e64 v31, 0, v32, s[10:11]
	v_add_f32_e32 v17, v41, v43
	v_add_f32_e32 v6, v6, v13
	v_add_f32_e32 v11, v14, v11
	v_add_f32_e32 v14, v20, v17
	v_add_f32_e32 v6, v31, v6
	v_max_f32_e32 v1, 0, v14
	v_max_f32_e32 v13, 0, v6
	v_cndmask_b32_e32 v6, 0, v25, vcc
	v_cndmask_b32_e64 v14, 0, v29, s[4:5]
	v_cndmask_b32_e64 v32, 0, v33, s[10:11]
	v_add_f32_e32 v6, v6, v14
	v_add_f32_e32 v6, v32, v6
	v_max_f32_e32 v16, 0, v6
	v_cndmask_b32_e32 v6, 0, v46, vcc
	v_cndmask_b32_e64 v14, 0, v50, s[4:5]
	v_cndmask_b32_e64 v33, 0, v34, s[10:11]
	v_add_f32_e32 v6, v6, v14
	v_add_f32_e32 v6, v33, v6
	v_max_f32_e32 v17, 0, v6
	v_cndmask_b32_e32 v6, 0, v47, vcc
	v_cndmask_b32_e64 v14, 0, v51, s[4:5]
	v_cndmask_b32_e64 v34, 0, v35, s[10:11]
	v_add_f32_e32 v6, v6, v14
	v_add_f32_e32 v6, v34, v6
	v_max_f32_e32 v14, 0, v6
	v_cndmask_b32_e32 v6, 0, v48, vcc
	v_cndmask_b32_e64 v15, 0, v52, s[4:5]
	v_cndmask_b32_e64 v35, 0, v36, s[10:11]
	v_add_f32_e32 v6, v6, v15
	v_add_f32_e32 v6, v35, v6
	v_max_f32_e32 v15, 0, v6
	v_cndmask_b32_e32 v6, 0, v49, vcc
	v_cndmask_b32_e64 v20, 0, v53, s[4:5]
	v_cndmask_b32_e64 v36, 0, v37, s[10:11]
	v_add_f32_e32 v6, v6, v20
	v_add_f32_e32 v6, v36, v6
	v_max_f32_e32 v20, 0, v6
	v_lshlrev_b32_e32 v6, 1, v64
	v_lshl_add_u64 v[6:7], v[8:9], 0, v[6:7]
	s_mov_b64 s[4:5], 0x2000000
	v_max_f32_e32 v11, 0, v11
	v_lshl_add_u64 v[6:7], v[6:7], 0, s[4:5]
	v_cmp_lt_u32_e32 vcc, 1, v65
	s_and_saveexec_b64 s[4:5], vcc
	s_xor_b64 s[4:5], exec, s[4:5]
	s_cbranch_execz .LBB0_6
	v_cvt_pk_f16_f32 v25, v3, v1
	v_cvt_pk_f16_f32 v24, v11, v2
	v_cvt_pk_f16_f32 v23, v5, v10
	v_cvt_pk_f16_f32 v22, v18, v4
	v_cvt_pk_f16_f32 v5, v15, v20
	v_cvt_pk_f16_f32 v4, v17, v14
	v_cvt_pk_f16_f32 v3, v13, v16
	v_cvt_pk_f16_f32 v2, v19, v12
	global_store_dwordx4 v[6:7], v[22:25], off sc1
	global_store_dwordx4 v[6:7], v[2:5], off offset:2048 sc1
.LBB0_6:
	s_andn2_saveexec_b64 s[4:5], s[4:5]
	s_cbranch_execz .LBB0_8
	v_add_f32_e32 v8, v18, v19
	v_add_f32_e32 v1, v1, v20
	v_cvt_f16_f32_e32 v8, v8
	v_cvt_f16_f32_e32 v1, v1
	v_pk_add_f32 v[4:5], v[4:5], v[12:13]
	v_pk_add_f32 v[10:11], v[10:11], v[16:17]
	v_pk_add_f32 v[2:3], v[2:3], v[14:15]
	v_cvt_pk_f16_f32 v4, v4, v5
	v_cvt_pk_f16_f32 v5, v10, v11
	v_cvt_pk_f16_f32 v2, v2, v3
	v_pack_b32_f16 v8, v8, v4
	v_alignbit_b32 v9, v5, v4, 16
	v_alignbit_b32 v10, v2, v5, 16
	v_alignbit_b32 v11, v1, v2, 16
	global_store_dwordx4 v[6:7], v[8:11], off sc1

.LBB0_15:
	s_lshl_b32 s7, s3, 2
	s_lshl_b32 s3, s3, 6
	s_and_b32 s3, s3, 0x3c0
	v_and_b32_e32 v1, 63, v0
	v_or_b32_e32 v16, s3, v1
	s_and_b32 s7, s7, 0x3c0
	v_lshrrev_b32_e32 v17, 6, v0
	v_min_u32_e32 v2, 0x3e8, v16
	v_lshlrev_b32_e32 v2, 2, v2
	v_mov_b32_e32 v3, 0
	v_or_b32_e32 v18, s7, v17
	v_lshl_add_u64 v[4:5], s[4:5], 0, v[2:3]
	v_mul_u32_u24_e32 v2, 0xfa4, v18
	v_lshl_add_u64 v[6:7], v[4:5], 0, v[2:3]
	v_or_b32_e32 v2, 4, v18
	v_mul_u32_u24_e32 v2, 0xfa4, v2
	v_lshl_add_u64 v[8:9], v[4:5], 0, v[2:3]
	v_or_b32_e32 v2, 8, v18
	v_mul_u32_u24_e32 v2, 0xfa4, v2
	v_lshl_add_u64 v[10:11], v[4:5], 0, v[2:3]
	v_or_b32_e32 v2, 12, v18
	v_mul_u32_u24_e32 v2, 0xfa4, v2
	global_load_dword v19, v[6:7], off
	global_load_dword v20, v[8:9], off
	global_load_dword v21, v[10:11], off
	v_lshl_add_u64 v[6:7], v[4:5], 0, v[2:3]
	v_or_b32_e32 v2, 16, v18
	v_mul_u32_u24_e32 v2, 0xfa4, v2
	v_lshl_add_u64 v[8:9], v[4:5], 0, v[2:3]
	v_or_b32_e32 v2, 20, v18
	v_mul_u32_u24_e32 v2, 0xfa4, v2
	v_lshl_add_u64 v[10:11], v[4:5], 0, v[2:3]
	v_or_b32_e32 v2, 24, v18
	v_mul_u32_u24_e32 v2, 0xfa4, v2
	v_or_b32_e32 v22, 28, v18
	v_lshl_add_u64 v[12:13], v[4:5], 0, v[2:3]
	v_mul_u32_u24_e32 v2, 0xfa4, v22
	v_lshl_add_u64 v[14:15], v[4:5], 0, v[2:3]
	global_load_dword v23, v[6:7], off
	global_load_dword v24, v[8:9], off
	global_load_dword v25, v[10:11], off
	global_load_dword v26, v[12:13], off
	global_load_dword v27, v[14:15], off
	v_or_b32_e32 v10, 32, v18
	v_mul_u32_u24_e32 v2, 0xfa4, v10
	v_or_b32_e32 v12, 36, v18
	v_lshl_add_u64 v[6:7], v[4:5], 0, v[2:3]
	v_mul_u32_u24_e32 v2, 0xfa4, v12
	v_or_b32_e32 v13, 40, v18
	global_load_dword v11, v[6:7], off
	v_lshl_add_u64 v[6:7], v[4:5], 0, v[2:3]
	v_min_u32_e32 v2, 0x3e8, v13
	v_mul_u32_u24_e32 v2, 0xfa4, v2
	v_or_b32_e32 v28, 44, v18
	v_lshl_add_u64 v[8:9], v[4:5], 0, v[2:3]
	v_min_u32_e32 v2, 0x3e8, v28
	v_mul_u32_u24_e32 v2, 0xfa4, v2
	v_or_b32_e32 v29, 48, v18
	global_load_dword v14, v[6:7], off
	global_load_dword v15, v[8:9], off
	v_lshl_add_u64 v[6:7], v[4:5], 0, v[2:3]
	v_min_u32_e32 v2, 0x3e8, v29
	v_mul_u32_u24_e32 v2, 0xfa4, v2
	v_lshl_add_u64 v[8:9], v[4:5], 0, v[2:3]
	global_load_dword v30, v[6:7], off
	global_load_dword v31, v[8:9], off
	v_or_b32_e32 v8, 52, v18
	v_min_u32_e32 v2, 0x3e8, v8
	v_mul_u32_u24_e32 v2, 0xfa4, v2
	v_or_b32_e32 v32, 56, v18
	v_lshl_add_u64 v[6:7], v[4:5], 0, v[2:3]
	v_min_u32_e32 v2, 0x3e8, v32
	global_load_dword v9, v[6:7], off
	v_mul_u32_u24_e32 v2, 0xfa4, v2
	v_lshl_add_u64 v[6:7], v[4:5], 0, v[2:3]
	global_load_dword v6, v[6:7], off
	v_or_b32_e32 v7, 60, v18
	v_min_u32_e32 v2, 0x3e8, v7
	v_mul_u32_u24_e32 v2, 0xfa4, v2
	v_lshl_add_u64 v[4:5], v[4:5], 0, v[2:3]
	global_load_dword v2, v[4:5], off
	s_movk_i32 s12, 0x3e9
	v_mul_u32_u24_e32 v4, 0x104, v17
	v_cmp_gt_u32_e32 vcc, s12, v16
	v_lshl_add_u32 v1, v1, 2, v4
	v_cmp_gt_u32_e64 s[4:5], s12, v22
	s_and_b64 s[4:5], s[4:5], vcc
	v_lshrrev_b32_e32 v16, 3, v0
	s_waitcnt vmcnt(15)
	v_cndmask_b32_e32 v4, 0, v19, vcc
	ds_write_b32 v1, v4
	s_waitcnt vmcnt(14)
	v_cndmask_b32_e32 v4, 0, v20, vcc
	ds_write_b32 v1, v4 offset:1040
	s_waitcnt vmcnt(13)
	v_cndmask_b32_e32 v4, 0, v21, vcc
	ds_write_b32 v1, v4 offset:2080
	s_waitcnt vmcnt(12)
	v_cndmask_b32_e32 v4, 0, v23, vcc
	ds_write_b32 v1, v4 offset:3120
	s_waitcnt vmcnt(11)
	v_cndmask_b32_e32 v4, 0, v24, vcc
	ds_write_b32 v1, v4 offset:4160
	s_waitcnt vmcnt(10)
	v_cndmask_b32_e32 v4, 0, v25, vcc
	ds_write_b32 v1, v4 offset:5200
	s_waitcnt vmcnt(9)
	v_cndmask_b32_e32 v4, 0, v26, vcc
	ds_write_b32 v1, v4 offset:6240
	s_waitcnt vmcnt(8)
	v_cndmask_b32_e64 v4, 0, v27, s[4:5]
	v_cmp_gt_u32_e64 s[4:5], s12, v10
	s_and_b64 s[4:5], s[4:5], vcc
	ds_write_b32 v1, v4 offset:7280
	s_waitcnt vmcnt(7)
	v_cndmask_b32_e64 v4, 0, v11, s[4:5]
	v_cmp_gt_u32_e64 s[4:5], s12, v12
	s_and_b64 s[4:5], s[4:5], vcc
	ds_write_b32 v1, v4 offset:8320
	s_waitcnt vmcnt(6)
	v_cndmask_b32_e64 v4, 0, v14, s[4:5]
	v_cmp_gt_u32_e64 s[4:5], s12, v13
	s_and_b64 s[4:5], s[4:5], vcc
	ds_write_b32 v1, v4 offset:9360
	s_waitcnt vmcnt(5)
	v_cndmask_b32_e64 v4, 0, v15, s[4:5]
	v_cmp_gt_u32_e64 s[4:5], s12, v28
	s_and_b64 s[4:5], s[4:5], vcc
	ds_write_b32 v1, v4 offset:10400
	s_waitcnt vmcnt(4)
	v_cndmask_b32_e64 v4, 0, v30, s[4:5]
	v_cmp_gt_u32_e64 s[4:5], s12, v29
	s_and_b64 s[4:5], s[4:5], vcc
	ds_write_b32 v1, v4 offset:11440
	s_waitcnt vmcnt(3)
	v_cndmask_b32_e64 v4, 0, v31, s[4:5]
	v_cmp_gt_u32_e64 s[4:5], s12, v8
	s_and_b64 s[4:5], s[4:5], vcc
	ds_write_b32 v1, v4 offset:12480
	s_waitcnt vmcnt(2)
	v_cndmask_b32_e64 v4, 0, v9, s[4:5]
	v_cmp_gt_u32_e64 s[4:5], s12, v32
	s_and_b64 s[4:5], s[4:5], vcc
	ds_write_b32 v1, v4 offset:13520
	s_waitcnt vmcnt(1)
	v_cndmask_b32_e64 v4, 0, v6, s[4:5]
	v_cmp_gt_u32_e64 s[4:5], s12, v7
	s_and_b64 vcc, s[4:5], vcc
	s_waitcnt lgkmcnt(0)
	s_add_u32 s10, s28, s10
	s_addc_u32 s11, s29, s11
	s_lshl_b64 s[4:5], s[8:9], 1
	s_add_u32 s4, s10, s4
	s_waitcnt vmcnt(0)
	v_cndmask_b32_e32 v2, 0, v2, vcc
	s_addc_u32 s5, s11, s5
	s_lshl_b32 s7, s7, 1
	ds_write_b32 v1, v4 offset:14560
	ds_write_b32 v1, v2 offset:15600
	v_and_b32_e32 v1, 7, v0
	s_add_u32 s4, s4, s7
	v_lshlrev_b32_e32 v4, 2, v16
	s_movk_i32 s7, 0x820
	v_mad_u32_u24 v6, v1, s7, v4
	s_addc_u32 s5, s5, 0
	v_lshlrev_b32_e32 v2, 4, v1
	v_add_u32_e32 v7, 0x400, v6
	s_waitcnt lgkmcnt(0)
	s_barrier
	ds_read2_b32 v[4:5], v7 offset0:134 offset1:199
	ds_read2_b32 v[8:9], v7 offset0:4 offset1:69
	ds_read2_b32 v[10:11], v6 offset0:130 offset1:195
	ds_read2_b32 v[12:13], v6 offset1:65
	v_lshl_add_u64 v[14:15], s[4:5], 0, v[2:3]
	v_or_b32_e32 v2, s3, v16
	v_mul_u32_u24_e32 v2, s6, v2
	v_lshlrev_b32_e32 v2, 1, v2
	s_waitcnt lgkmcnt(2)
	v_cvt_pk_f16_f32 v6, v8, v9
	v_lshl_add_u64 v[8:9], v[14:15], 0, v[2:3]
	v_or_b32_e32 v2, 0x100, v0
	v_lshrrev_b32_e32 v2, 3, v2
	v_cvt_pk_f16_f32 v7, v4, v5
	s_waitcnt lgkmcnt(1)
	v_cvt_pk_f16_f32 v5, v10, v11
	v_lshlrev_b32_e32 v10, 2, v2
	v_mad_u32_u24 v1, v1, s7, v10
	s_waitcnt lgkmcnt(0)
	v_cvt_pk_f16_f32 v4, v12, v13
	v_add_u32_e32 v12, 0x400, v1
	ds_read2_b32 v[10:11], v12 offset0:134 offset1:199
	ds_read2_b32 v[12:13], v12 offset0:4 offset1:69
	ds_read2_b32 v[16:17], v1 offset0:130 offset1:195
	ds_read2_b32 v[18:19], v1 offset1:65
	v_or_b32_e32 v1, s3, v2
	v_mul_u32_u24_e32 v1, s6, v1
	v_lshlrev_b32_e32 v2, 1, v1
	global_store_dwordx4 v[8:9], v[4:7], off sc1
	v_lshl_add_u64 v[2:3], v[14:15], 0, v[2:3]
	s_waitcnt lgkmcnt(3)
	v_cvt_pk_f16_f32 v7, v10, v11
	s_waitcnt lgkmcnt(2)
	v_cvt_pk_f16_f32 v6, v12, v13
	s_waitcnt lgkmcnt(1)
	v_cvt_pk_f16_f32 v5, v16, v17
	s_waitcnt lgkmcnt(0)
	v_cvt_pk_f16_f32 v4, v18, v19
	global_store_dwordx4 v[2:3], v[4:7], off sc1

_Z16gemm_glds_kernelILi2EEvPKDF16_PDF16_PKiS4_S1_S1_PKfiS6_Pc:
	s_load_dword s3, s[0:1], 0x38
	s_mov_b64 s[4:5], -1
	s_waitcnt lgkmcnt(0)
	s_cmp_lt_i32 s2, s3
	s_cbranch_scc1 .LBB2_2
	s_load_dwordx4 s[4:7], s[0:1], 0x40
	s_sub_i32 s3, s2, s3
	v_lshrrev_b32_e32 v1, 8, v0
	s_lshl_b32 s8, s3, 1
	v_or_b32_e32 v6, s8, v1
	s_bfe_u32 s8, s3, 0x180007
	v_mov_b32_e32 v4, 0x3d2844
	s_waitcnt lgkmcnt(0)
	v_mov_b64_e32 v[2:3], s[4:5]
	v_mad_u64_u32 v[4:5], s[4:5], s8, v4, v[2:3]
	v_lshlrev_b32_e32 v2, 6, v6
	v_and_b32_e32 v26, 0x3c0, v2
	v_and_b32_e32 v22, 63, v0
	s_lshl_b32 s3, s3, 3
	v_or_b32_e32 v23, v26, v22
	s_and_b32 s3, s3, 0x3c0
	v_bfe_u32 v24, v0, 6, 2
	v_min_u32_e32 v2, 0x3e8, v23
	v_lshlrev_b32_e32 v2, 2, v2
	v_mov_b32_e32 v3, 0
	v_or_b32_e32 v25, s3, v24
	v_lshl_add_u64 v[4:5], v[4:5], 0, v[2:3]
	v_mul_u32_u24_e32 v2, 0xfa4, v25
	v_lshl_add_u64 v[6:7], v[4:5], 0, v[2:3]
	v_or_b32_e32 v2, 4, v25
	v_mul_u32_u24_e32 v2, 0xfa4, v2
	v_lshl_add_u64 v[8:9], v[4:5], 0, v[2:3]
	v_or_b32_e32 v2, 8, v25
	v_mul_u32_u24_e32 v2, 0xfa4, v2
	v_lshl_add_u64 v[10:11], v[4:5], 0, v[2:3]
	v_or_b32_e32 v2, 12, v25
	v_mul_u32_u24_e32 v2, 0xfa4, v2
	v_lshl_add_u64 v[12:13], v[4:5], 0, v[2:3]
	v_or_b32_e32 v2, 16, v25
	v_mul_u32_u24_e32 v2, 0xfa4, v2
	v_lshl_add_u64 v[14:15], v[4:5], 0, v[2:3]
	v_or_b32_e32 v2, 20, v25
	v_mul_u32_u24_e32 v2, 0xfa4, v2
	v_lshl_add_u64 v[16:17], v[4:5], 0, v[2:3]
	v_or_b32_e32 v2, 24, v25
	v_mul_u32_u24_e32 v2, 0xfa4, v2
	v_lshl_add_u64 v[18:19], v[4:5], 0, v[2:3]
	v_or_b32_e32 v2, 28, v25
	v_mul_u32_u24_e32 v2, 0xfa4, v2
	v_lshl_add_u64 v[20:21], v[4:5], 0, v[2:3]
	v_or_b32_e32 v2, 32, v25
	v_mul_u32_u24_e32 v2, 0xfa4, v2
	global_load_dword v27, v[6:7], off
	global_load_dword v28, v[8:9], off
	global_load_dword v29, v[10:11], off
	global_load_dword v30, v[12:13], off
	global_load_dword v31, v[14:15], off
	global_load_dword v32, v[16:17], off
	global_load_dword v33, v[18:19], off
	global_load_dword v34, v[20:21], off
	v_lshl_add_u64 v[6:7], v[4:5], 0, v[2:3]
	v_or_b32_e32 v2, 36, v25
	v_mul_u32_u24_e32 v2, 0xfa4, v2
	v_or_b32_e32 v12, 40, v25
	v_lshl_add_u64 v[8:9], v[4:5], 0, v[2:3]
	v_min_u32_e32 v2, 0x3e8, v12
	v_mul_u32_u24_e32 v2, 0xfa4, v2
	v_lshl_add_u64 v[10:11], v[4:5], 0, v[2:3]
	global_load_dword v13, v[6:7], off
	global_load_dword v14, v[8:9], off
	global_load_dword v15, v[10:11], off
	v_or_b32_e32 v10, 44, v25
	v_min_u32_e32 v2, 0x3e8, v10
	v_mul_u32_u24_e32 v2, 0xfa4, v2
	v_or_b32_e32 v11, 48, v25
	v_lshl_add_u64 v[6:7], v[4:5], 0, v[2:3]
	v_min_u32_e32 v2, 0x3e8, v11
	v_mul_u32_u24_e32 v2, 0xfa4, v2
	v_lshl_add_u64 v[8:9], v[4:5], 0, v[2:3]
	global_load_dword v16, v[6:7], off
	global_load_dword v17, v[8:9], off
	v_or_b32_e32 v8, 52, v25
	v_min_u32_e32 v2, 0x3e8, v8
	v_mul_u32_u24_e32 v2, 0xfa4, v2
	v_or_b32_e32 v18, 56, v25
	v_lshl_add_u64 v[6:7], v[4:5], 0, v[2:3]
	v_min_u32_e32 v2, 0x3e8, v18
	v_mul_u32_u24_e32 v2, 0xfa4, v2
	global_load_dword v9, v[6:7], off
	v_lshl_add_u64 v[6:7], v[4:5], 0, v[2:3]
	global_load_dword v6, v[6:7], off
	v_or_b32_e32 v7, 60, v25
	v_min_u32_e32 v2, 0x3e8, v7
	v_mul_u32_u24_e32 v2, 0xfa4, v2
	v_lshl_add_u64 v[4:5], v[4:5], 0, v[2:3]
	global_load_dword v2, v[4:5], off
	s_movk_i32 s4, 0x4100
	s_movk_i32 s10, 0x3e9
	v_mad_u32_u24 v1, v1, s4, 0
	v_lshlrev_b32_e32 v4, 2, v22
	v_cmp_gt_u32_e32 vcc, s10, v23
	v_mul_u32_u24_e32 v19, 0x104, v24
	v_add3_u32 v4, v1, v4, v19
	v_cmp_gt_u32_e64 s[4:5], s10, v12
	s_and_b64 s[4:5], s[4:5], vcc
	s_mov_b32 s9, 0
	s_lshl_b64 s[8:9], s[8:9], 21
	s_waitcnt vmcnt(15)
	v_cndmask_b32_e32 v5, 0, v27, vcc
	ds_write_b32 v4, v5
	s_waitcnt vmcnt(14)
	v_cndmask_b32_e32 v5, 0, v28, vcc
	ds_write_b32 v4, v5 offset:1040
	s_waitcnt vmcnt(13)
	v_cndmask_b32_e32 v5, 0, v29, vcc
	ds_write_b32 v4, v5 offset:2080
	s_waitcnt vmcnt(12)
	v_cndmask_b32_e32 v5, 0, v30, vcc
	ds_write_b32 v4, v5 offset:3120
	s_waitcnt vmcnt(11)
	v_cndmask_b32_e32 v5, 0, v31, vcc
	ds_write_b32 v4, v5 offset:4160
	s_waitcnt vmcnt(10)
	v_cndmask_b32_e32 v5, 0, v32, vcc
	ds_write_b32 v4, v5 offset:5200
	s_waitcnt vmcnt(9)
	v_cndmask_b32_e32 v5, 0, v33, vcc
	ds_write_b32 v4, v5 offset:6240
	s_waitcnt vmcnt(8)
	v_cndmask_b32_e32 v5, 0, v34, vcc
	ds_write_b32 v4, v5 offset:7280
	s_waitcnt vmcnt(7)
	v_cndmask_b32_e32 v5, 0, v13, vcc
	ds_write_b32 v4, v5 offset:8320
	s_waitcnt vmcnt(6)
	v_cndmask_b32_e32 v5, 0, v14, vcc
	ds_write_b32 v4, v5 offset:9360
	s_waitcnt vmcnt(5)
	v_cndmask_b32_e64 v5, 0, v15, s[4:5]
	v_cmp_gt_u32_e64 s[4:5], s10, v10
	s_and_b64 s[4:5], s[4:5], vcc
	ds_write_b32 v4, v5 offset:10400
	s_waitcnt vmcnt(4)
	v_cndmask_b32_e64 v5, 0, v16, s[4:5]
	v_cmp_gt_u32_e64 s[4:5], s10, v11
	s_and_b64 s[4:5], s[4:5], vcc
	ds_write_b32 v4, v5 offset:11440
	s_waitcnt vmcnt(3)
	v_cndmask_b32_e64 v5, 0, v17, s[4:5]
	v_cmp_gt_u32_e64 s[4:5], s10, v8
	s_and_b64 s[4:5], s[4:5], vcc
	ds_write_b32 v4, v5 offset:12480
	s_waitcnt vmcnt(2)
	v_cndmask_b32_e64 v5, 0, v9, s[4:5]
	v_cmp_gt_u32_e64 s[4:5], s10, v18
	s_and_b64 s[4:5], s[4:5], vcc
	ds_write_b32 v4, v5 offset:13520
	s_waitcnt vmcnt(1)
	v_cndmask_b32_e64 v5, 0, v6, s[4:5]
	v_cmp_gt_u32_e64 s[4:5], s10, v7
	s_and_b64 vcc, s[4:5], vcc
	s_waitcnt vmcnt(0)
	v_cndmask_b32_e32 v2, 0, v2, vcc
	s_add_u32 s4, s6, s8
	ds_write_b32 v4, v2 offset:15600
	s_addc_u32 s5, s7, s9
	v_lshlrev_b32_e32 v2, 3, v0
	s_lshl_b32 s3, s3, 1
	v_and_b32_e32 v6, 56, v2
	s_add_u32 s4, s4, s3
	s_addc_u32 s5, s5, 0
	v_lshlrev_b32_e32 v2, 1, v6
	ds_write_b32 v4, v5 offset:14560
	v_lshl_add_u64 v[4:5], s[4:5], 0, v[2:3]
	v_bfe_u32 v2, v0, 3, 5
	v_lshlrev_b32_e32 v7, 2, v2
	v_mul_u32_u24_e32 v6, 0x104, v6
	v_add3_u32 v1, v1, v7, v6
	v_add_u32_e32 v6, 0x400, v1
	s_waitcnt lgkmcnt(0)
	s_barrier
	ds_read2_b32 v[8:9], v1 offset1:32
	ds_read2_b32 v[10:11], v1 offset0:130 offset1:162
	ds_read2_b32 v[12:13], v6 offset0:4 offset1:36
	ds_read2_b32 v[14:15], v6 offset0:134 offset1:166
	ds_read2_b32 v[16:17], v6 offset0:199 offset1:231
	ds_read2_b32 v[18:19], v6 offset0:69 offset1:101
	ds_read2_b32 v[20:21], v1 offset0:195 offset1:227
	ds_read2_b32 v[22:23], v1 offset0:65 offset1:97
	s_mov_b64 s[4:5], 0x800000
	v_or_b32_e32 v1, v26, v2
	v_lshl_add_u64 v[24:25], v[4:5], 0, s[4:5]
	v_lshlrev_b32_e32 v2, 11, v1
	s_waitcnt lgkmcnt(3)
	v_cvt_pk_f16_f32 v7, v14, v16
	s_waitcnt lgkmcnt(2)
	v_cvt_pk_f16_f32 v6, v12, v18
	s_waitcnt lgkmcnt(1)
	v_cvt_pk_f16_f32 v5, v10, v20
	s_waitcnt lgkmcnt(0)
	v_cvt_pk_f16_f32 v4, v8, v22
	v_lshl_add_u64 v[26:27], v[24:25], 0, v[2:3]
	v_or_b32_e32 v2, 0x10000, v2
	global_store_dwordx4 v[26:27], v[4:7], off sc1
	v_lshl_add_u64 v[2:3], v[24:25], 0, v[2:3]
	s_mov_b64 s[4:5], 0
	v_cvt_pk_f16_f32 v7, v15, v17
	v_cvt_pk_f16_f32 v6, v13, v19
	v_cvt_pk_f16_f32 v5, v11, v21
	v_cvt_pk_f16_f32 v4, v9, v23
	global_store_dwordx4 v[2:3], v[4:7], off sc1
